# MoE gate/up: gather-index table build batched (8 count loads together, then 8 rowmap loads, branch-free) in both layers
# speedup vs baseline: 1.0178x; 1.0029x over previous
; #define LAS __attribute__((address_space(3)))
;     __device__ __forceinline__ void build_units(LAS int* tab) const {
;     ...
;         if (UP && gtab != nullptr) {
;             LAS int* gt = (LAS int*)gtab;
;             for (int i0 = 0; i0 < 16; i0 += 2) { const int i = i0 + (int)(threadIdx.x >> 8), r = (int)threadIdx.x & 255;
;                 if (tab[i * 4 + 3]) { const int mtg = tab[i * 4 + 0], e = tab[i * 4 + 2], mt = mtg - toff[e];
;                     int v; if (e < N_EXPERTS) { const int n = (int)cnt[e] - mt * 256; v = (r < n) ? rowmap[(size_t)e * T + mt * 256 + r] : 0; } else v = mt * 256 + r;
;                     gt[i * 256 + r] = v; } }
.LBB0_1391:
	s_or_b64 exec, exec, s[4:5]
	s_waitcnt vmcnt(14)
	v_lshrrev_b32_e32 v7, 8, v0
	v_lshlrev_b32_e32 v1, 4, v7
	v_add_u32_e32 v2, s56, v1
	s_waitcnt lgkmcnt(0)
	s_barrier
	s_add_u32 s22, s18, 0x1000
	s_addc_u32 s23, s19, 0
	s_add_u32 s26, s6, 0x35600000
	s_addc_u32 s27, s7, 0
	s_add_i32 s57, s0, 0x20000
	v_and_b32_e32 v6, 0xff, v0
	v_lshl_add_u32 v9, v6, 2, s57
	v_lshl_add_u32 v9, v7, 10, v9
	ds_read2_b32 v[20:21], v2 offset0:0 offset1:2
	ds_read_b32 v10, v2 offset:12
	ds_read2_b32 v[22:23], v2 offset0:8 offset1:10
	ds_read_b32 v11, v2 offset:44
	ds_read2_b32 v[24:25], v2 offset0:16 offset1:18
	ds_read_b32 v12, v2 offset:76
	ds_read2_b32 v[26:27], v2 offset0:24 offset1:26
	ds_read_b32 v13, v2 offset:108
	s_waitcnt lgkmcnt(0)
	ds_read2_b32 v[28:29], v2 offset0:32 offset1:34
	ds_read_b32 v14, v2 offset:140
	ds_read2_b32 v[30:31], v2 offset0:40 offset1:42
	ds_read_b32 v15, v2 offset:172
	ds_read2_b32 v[32:33], v2 offset0:48 offset1:50
	ds_read_b32 v16, v2 offset:204
	ds_read2_b32 v[34:35], v2 offset0:56 offset1:58
	ds_read_b32 v17, v2 offset:236
	s_waitcnt lgkmcnt(0)
	v_lshl_add_u32 v40, v21, 2, s51
	ds_read_b32 v40, v40
	v_lshl_add_u32 v41, v23, 2, s51
	ds_read_b32 v41, v41
	v_lshl_add_u32 v42, v25, 2, s51
	ds_read_b32 v42, v42
	v_lshl_add_u32 v43, v27, 2, s51
	ds_read_b32 v43, v43
	v_lshl_add_u32 v44, v29, 2, s51
	ds_read_b32 v44, v44
	v_lshl_add_u32 v45, v31, 2, s51
	ds_read_b32 v45, v45
	v_lshl_add_u32 v46, v33, 2, s51
	ds_read_b32 v46, v46
	v_lshl_add_u32 v47, v35, 2, s51
	ds_read_b32 v47, v47
	s_waitcnt lgkmcnt(0)
	v_sub_u32_e32 v20, v20, v40
	v_lshlrev_b32_e32 v56, 2, v21
	global_load_dword v48, v56, s[22:23]
	v_sub_u32_e32 v22, v22, v41
	v_lshlrev_b32_e32 v57, 2, v23
	global_load_dword v49, v57, s[22:23]
	v_sub_u32_e32 v24, v24, v42
	v_lshlrev_b32_e32 v58, 2, v25
	global_load_dword v50, v58, s[22:23]
	v_sub_u32_e32 v26, v26, v43
	v_lshlrev_b32_e32 v59, 2, v27
	global_load_dword v51, v59, s[22:23]
	v_sub_u32_e32 v28, v28, v44
	v_lshlrev_b32_e32 v60, 2, v29
	global_load_dword v52, v60, s[22:23]
	v_sub_u32_e32 v30, v30, v45
	v_lshlrev_b32_e32 v61, 2, v31
	global_load_dword v53, v61, s[22:23]
	v_sub_u32_e32 v32, v32, v46
	v_lshlrev_b32_e32 v62, 2, v33
	global_load_dword v54, v62, s[22:23]
	v_sub_u32_e32 v34, v34, v47
	v_lshlrev_b32_e32 v63, 2, v35
	global_load_dword v55, v63, s[22:23]
	s_waitcnt vmcnt(0)
;     __device__ __forceinline__ void build_units(LAS int* tab) const {
;     ...
;                 if (tab[i * 4 + 3]) { const int mtg = tab[i * 4 + 0], e = tab[i * 4 + 2], mt = mtg - toff[e];
;                     int v; if (e < N_EXPERTS) { const int n = (int)cnt[e] - mt * 256; v = (r < n) ? rowmap[(size_t)e * T + mt * 256 + r] : 0; } else v = mt * 256 + r;
;                     gt[i * 256 + r] = v; } }
	v_lshlrev_b32_e32 v40, 8, v20
	v_sub_u32_e32 v48, v48, v40
	v_add_u32_e32 v40, v40, v6
	v_cmp_lt_i32_e32 vcc, v6, v48
	v_cmp_gt_i32_e64 s[14:15], 64, v21
	s_and_b64 vcc, vcc, s[14:15]
	v_cndmask_b32_e64 v64, 0, 1, vcc
	v_cndmask_b32_e32 v56, 0, v40, vcc
	v_lshl_add_u32 v56, v21, 14, v56
	v_lshlrev_b32_e32 v56, 2, v56
	global_load_dword v48, v56, s[26:27]
	v_lshlrev_b32_e32 v41, 8, v22
	v_sub_u32_e32 v49, v49, v41
	v_add_u32_e32 v41, v41, v6
	v_cmp_lt_i32_e32 vcc, v6, v49
	v_cmp_gt_i32_e64 s[14:15], 64, v23
	s_and_b64 vcc, vcc, s[14:15]
	v_cndmask_b32_e64 v65, 0, 1, vcc
	v_cndmask_b32_e32 v57, 0, v41, vcc
	v_lshl_add_u32 v57, v23, 14, v57
	v_lshlrev_b32_e32 v57, 2, v57
	global_load_dword v49, v57, s[26:27]
	v_lshlrev_b32_e32 v42, 8, v24
	v_sub_u32_e32 v50, v50, v42
	v_add_u32_e32 v42, v42, v6
	v_cmp_lt_i32_e32 vcc, v6, v50
	v_cmp_gt_i32_e64 s[14:15], 64, v25
	s_and_b64 vcc, vcc, s[14:15]
	v_cndmask_b32_e64 v66, 0, 1, vcc
	v_cndmask_b32_e32 v58, 0, v42, vcc
	v_lshl_add_u32 v58, v25, 14, v58
	v_lshlrev_b32_e32 v58, 2, v58
	global_load_dword v50, v58, s[26:27]
	v_lshlrev_b32_e32 v43, 8, v26
	v_sub_u32_e32 v51, v51, v43
	v_add_u32_e32 v43, v43, v6
	v_cmp_lt_i32_e32 vcc, v6, v51
	v_cmp_gt_i32_e64 s[14:15], 64, v27
	s_and_b64 vcc, vcc, s[14:15]
	v_cndmask_b32_e64 v67, 0, 1, vcc
	v_cndmask_b32_e32 v59, 0, v43, vcc
	v_lshl_add_u32 v59, v27, 14, v59
	v_lshlrev_b32_e32 v59, 2, v59
	global_load_dword v51, v59, s[26:27]
	v_lshlrev_b32_e32 v44, 8, v28
	v_sub_u32_e32 v52, v52, v44
	v_add_u32_e32 v44, v44, v6
	v_cmp_lt_i32_e32 vcc, v6, v52
	v_cmp_gt_i32_e64 s[14:15], 64, v29
	s_and_b64 vcc, vcc, s[14:15]
	v_cndmask_b32_e64 v68, 0, 1, vcc
	v_cndmask_b32_e32 v60, 0, v44, vcc
	v_lshl_add_u32 v60, v29, 14, v60
	v_lshlrev_b32_e32 v60, 2, v60
	global_load_dword v52, v60, s[26:27]
	v_lshlrev_b32_e32 v45, 8, v30
	v_sub_u32_e32 v53, v53, v45
	v_add_u32_e32 v45, v45, v6
	v_cmp_lt_i32_e32 vcc, v6, v53
	v_cmp_gt_i32_e64 s[14:15], 64, v31
	s_and_b64 vcc, vcc, s[14:15]
	v_cndmask_b32_e64 v69, 0, 1, vcc
	v_cndmask_b32_e32 v61, 0, v45, vcc
	v_lshl_add_u32 v61, v31, 14, v61
	v_lshlrev_b32_e32 v61, 2, v61
	global_load_dword v53, v61, s[26:27]
	v_lshlrev_b32_e32 v46, 8, v32
	v_sub_u32_e32 v54, v54, v46
	v_add_u32_e32 v46, v46, v6
	v_cmp_lt_i32_e32 vcc, v6, v54
	v_cmp_gt_i32_e64 s[14:15], 64, v33
	s_and_b64 vcc, vcc, s[14:15]
	v_cndmask_b32_e64 v70, 0, 1, vcc
	v_cndmask_b32_e32 v62, 0, v46, vcc
	v_lshl_add_u32 v62, v33, 14, v62
	v_lshlrev_b32_e32 v62, 2, v62
	global_load_dword v54, v62, s[26:27]
	v_lshlrev_b32_e32 v47, 8, v34
	v_sub_u32_e32 v55, v55, v47
	v_add_u32_e32 v47, v47, v6
	v_cmp_lt_i32_e32 vcc, v6, v55
	v_cmp_gt_i32_e64 s[14:15], 64, v35
	s_and_b64 vcc, vcc, s[14:15]
	v_cndmask_b32_e64 v71, 0, 1, vcc
	v_cndmask_b32_e32 v63, 0, v47, vcc
	v_lshl_add_u32 v63, v35, 14, v63
	v_lshlrev_b32_e32 v63, 2, v63
	global_load_dword v55, v63, s[26:27]
	s_waitcnt vmcnt(0)
	v_cmp_ne_u32_e32 vcc, 0, v64
	s_nop 1
	v_cndmask_b32_e32 v48, 0, v48, vcc
	v_cmp_lt_i32_e32 vcc, 63, v21
	s_nop 1
	v_cndmask_b32_e32 v48, v48, v40, vcc
	v_cmp_ne_u32_e32 vcc, 0, v10
	s_and_saveexec_b64 s[14:15], vcc
	ds_write_b32 v9, v48
	s_mov_b64 exec, s[14:15]
	v_cmp_ne_u32_e32 vcc, 0, v65
	s_nop 1
	v_cndmask_b32_e32 v49, 0, v49, vcc
	v_cmp_lt_i32_e32 vcc, 63, v23
	s_nop 1
	v_cndmask_b32_e32 v49, v49, v41, vcc
	v_cmp_ne_u32_e32 vcc, 0, v11
	s_and_saveexec_b64 s[14:15], vcc
	ds_write_b32 v9, v49 offset:2048
	s_mov_b64 exec, s[14:15]
	v_cmp_ne_u32_e32 vcc, 0, v66
	s_nop 1
	v_cndmask_b32_e32 v50, 0, v50, vcc
	v_cmp_lt_i32_e32 vcc, 63, v25
	s_nop 1
	v_cndmask_b32_e32 v50, v50, v42, vcc
	v_cmp_ne_u32_e32 vcc, 0, v12
	s_and_saveexec_b64 s[14:15], vcc
	ds_write_b32 v9, v50 offset:4096
	s_mov_b64 exec, s[14:15]
	v_cmp_ne_u32_e32 vcc, 0, v67
	s_nop 1
	v_cndmask_b32_e32 v51, 0, v51, vcc
	v_cmp_lt_i32_e32 vcc, 63, v27
	s_nop 1
	v_cndmask_b32_e32 v51, v51, v43, vcc
	v_cmp_ne_u32_e32 vcc, 0, v13
	s_and_saveexec_b64 s[14:15], vcc
	ds_write_b32 v9, v51 offset:6144
	s_mov_b64 exec, s[14:15]
	v_cmp_ne_u32_e32 vcc, 0, v68
	s_nop 1
	v_cndmask_b32_e32 v52, 0, v52, vcc
	v_cmp_lt_i32_e32 vcc, 63, v29
	s_nop 1
	v_cndmask_b32_e32 v52, v52, v44, vcc
	v_cmp_ne_u32_e32 vcc, 0, v14
	s_and_saveexec_b64 s[14:15], vcc
	ds_write_b32 v9, v52 offset:8192
	s_mov_b64 exec, s[14:15]
	v_cmp_ne_u32_e32 vcc, 0, v69
	s_nop 1
	v_cndmask_b32_e32 v53, 0, v53, vcc
	v_cmp_lt_i32_e32 vcc, 63, v31
	s_nop 1
	v_cndmask_b32_e32 v53, v53, v45, vcc
	v_cmp_ne_u32_e32 vcc, 0, v15
	s_and_saveexec_b64 s[14:15], vcc
	ds_write_b32 v9, v53 offset:10240
	s_mov_b64 exec, s[14:15]
	v_cmp_ne_u32_e32 vcc, 0, v70
	s_nop 1
	v_cndmask_b32_e32 v54, 0, v54, vcc
	v_cmp_lt_i32_e32 vcc, 63, v33
	s_nop 1
	v_cndmask_b32_e32 v54, v54, v46, vcc
	v_cmp_ne_u32_e32 vcc, 0, v16
	s_and_saveexec_b64 s[14:15], vcc
	ds_write_b32 v9, v54 offset:12288
	s_mov_b64 exec, s[14:15]
	v_cmp_ne_u32_e32 vcc, 0, v71
	s_nop 1
	v_cndmask_b32_e32 v55, 0, v55, vcc
	v_cmp_lt_i32_e32 vcc, 63, v35
	s_nop 1
	v_cndmask_b32_e32 v55, v55, v47, vcc
	v_cmp_ne_u32_e32 vcc, 0, v17
	s_and_saveexec_b64 s[14:15], vcc
	ds_write_b32 v9, v55 offset:14336
	s_mov_b64 exec, s[14:15]

; #define LAS __attribute__((address_space(3)))
;     __device__ __forceinline__ void build_units(LAS int* tab) const {
;     ...
;         if (UP && gtab != nullptr) {
;             LAS int* gt = (LAS int*)gtab;
;             for (int i0 = 0; i0 < 16; i0 += 2) { const int i = i0 + (int)(threadIdx.x >> 8), r = (int)threadIdx.x & 255;
;                 if (tab[i * 4 + 3]) { const int mtg = tab[i * 4 + 0], e = tab[i * 4 + 2], mt = mtg - toff[e];
;                     int v; if (e < N_EXPERTS) { const int n = (int)cnt[e] - mt * 256; v = (r < n) ? rowmap[(size_t)e * T + mt * 256 + r] : 0; } else v = mt * 256 + r;
;                     gt[i * 256 + r] = v; } }
.LBB0_2956:
	s_or_b64 exec, exec, s[10:11]
	v_lshrrev_b32_e32 v7, 8, v0
	v_lshlrev_b32_e32 v1, 4, v7
	v_add_u32_e32 v2, s1, v1
	s_waitcnt lgkmcnt(0)
	s_barrier
	s_add_u32 s10, s4, 0x1100
	s_addc_u32 s11, s5, 0
	s_add_u32 s12, s6, 0x35600000
	s_addc_u32 s13, s7, 0
	s_add_i32 s2, s34, 0x20000
	v_and_b32_e32 v6, 0xff, v0
	v_lshl_add_u32 v9, v6, 2, s2
	v_lshl_add_u32 v9, v7, 10, v9
	ds_read2_b32 v[20:21], v2 offset0:0 offset1:2
	ds_read_b32 v10, v2 offset:12
	ds_read2_b32 v[22:23], v2 offset0:8 offset1:10
	ds_read_b32 v11, v2 offset:44
	ds_read2_b32 v[24:25], v2 offset0:16 offset1:18
	ds_read_b32 v12, v2 offset:76
	ds_read2_b32 v[26:27], v2 offset0:24 offset1:26
	ds_read_b32 v13, v2 offset:108
	s_waitcnt lgkmcnt(0)
	ds_read2_b32 v[28:29], v2 offset0:32 offset1:34
	ds_read_b32 v14, v2 offset:140
	ds_read2_b32 v[30:31], v2 offset0:40 offset1:42
	ds_read_b32 v15, v2 offset:172
	ds_read2_b32 v[32:33], v2 offset0:48 offset1:50
	ds_read_b32 v16, v2 offset:204
	ds_read2_b32 v[34:35], v2 offset0:56 offset1:58
	ds_read_b32 v17, v2 offset:236
	s_waitcnt lgkmcnt(0)
	v_lshl_add_u32 v40, v21, 2, s0
	ds_read_b32 v40, v40
	v_lshl_add_u32 v41, v23, 2, s0
	ds_read_b32 v41, v41
	v_lshl_add_u32 v42, v25, 2, s0
	ds_read_b32 v42, v42
	v_lshl_add_u32 v43, v27, 2, s0
	ds_read_b32 v43, v43
	v_lshl_add_u32 v44, v29, 2, s0
	ds_read_b32 v44, v44
	v_lshl_add_u32 v45, v31, 2, s0
	ds_read_b32 v45, v45
	v_lshl_add_u32 v46, v33, 2, s0
	ds_read_b32 v46, v46
	v_lshl_add_u32 v47, v35, 2, s0
	ds_read_b32 v47, v47
	s_waitcnt lgkmcnt(0)
	v_sub_u32_e32 v20, v20, v40
	v_lshlrev_b32_e32 v56, 2, v21
	global_load_dword v48, v56, s[10:11]
	v_sub_u32_e32 v22, v22, v41
	v_lshlrev_b32_e32 v57, 2, v23
	global_load_dword v49, v57, s[10:11]
	v_sub_u32_e32 v24, v24, v42
	v_lshlrev_b32_e32 v58, 2, v25
	global_load_dword v50, v58, s[10:11]
	v_sub_u32_e32 v26, v26, v43
	v_lshlrev_b32_e32 v59, 2, v27
	global_load_dword v51, v59, s[10:11]
	v_sub_u32_e32 v28, v28, v44
	v_lshlrev_b32_e32 v60, 2, v29
	global_load_dword v52, v60, s[10:11]
	v_sub_u32_e32 v30, v30, v45
	v_lshlrev_b32_e32 v61, 2, v31
	global_load_dword v53, v61, s[10:11]
	v_sub_u32_e32 v32, v32, v46
	v_lshlrev_b32_e32 v62, 2, v33
	global_load_dword v54, v62, s[10:11]
	v_sub_u32_e32 v34, v34, v47
	v_lshlrev_b32_e32 v63, 2, v35
	global_load_dword v55, v63, s[10:11]
	s_waitcnt vmcnt(0)
;     __device__ __forceinline__ void build_units(LAS int* tab) const {
;     ...
;                 if (tab[i * 4 + 3]) { const int mtg = tab[i * 4 + 0], e = tab[i * 4 + 2], mt = mtg - toff[e];
;                     int v; if (e < N_EXPERTS) { const int n = (int)cnt[e] - mt * 256; v = (r < n) ? rowmap[(size_t)e * T + mt * 256 + r] : 0; } else v = mt * 256 + r;
;                     gt[i * 256 + r] = v; } }
	v_lshlrev_b32_e32 v40, 8, v20
	v_sub_u32_e32 v48, v48, v40
	v_add_u32_e32 v40, v40, v6
	v_cmp_lt_i32_e32 vcc, v6, v48
	v_cmp_gt_i32_e64 s[16:17], 64, v21
	s_and_b64 vcc, vcc, s[16:17]
	v_cndmask_b32_e64 v64, 0, 1, vcc
	v_cndmask_b32_e32 v56, 0, v40, vcc
	v_lshl_add_u32 v56, v21, 14, v56
	v_lshlrev_b32_e32 v56, 2, v56
	global_load_dword v48, v56, s[12:13]
	v_lshlrev_b32_e32 v41, 8, v22
	v_sub_u32_e32 v49, v49, v41
	v_add_u32_e32 v41, v41, v6
	v_cmp_lt_i32_e32 vcc, v6, v49
	v_cmp_gt_i32_e64 s[16:17], 64, v23
	s_and_b64 vcc, vcc, s[16:17]
	v_cndmask_b32_e64 v65, 0, 1, vcc
	v_cndmask_b32_e32 v57, 0, v41, vcc
	v_lshl_add_u32 v57, v23, 14, v57
	v_lshlrev_b32_e32 v57, 2, v57
	global_load_dword v49, v57, s[12:13]
	v_lshlrev_b32_e32 v42, 8, v24
	v_sub_u32_e32 v50, v50, v42
	v_add_u32_e32 v42, v42, v6
	v_cmp_lt_i32_e32 vcc, v6, v50
	v_cmp_gt_i32_e64 s[16:17], 64, v25
	s_and_b64 vcc, vcc, s[16:17]
	v_cndmask_b32_e64 v66, 0, 1, vcc
	v_cndmask_b32_e32 v58, 0, v42, vcc
	v_lshl_add_u32 v58, v25, 14, v58
	v_lshlrev_b32_e32 v58, 2, v58
	global_load_dword v50, v58, s[12:13]
	v_lshlrev_b32_e32 v43, 8, v26
	v_sub_u32_e32 v51, v51, v43
	v_add_u32_e32 v43, v43, v6
	v_cmp_lt_i32_e32 vcc, v6, v51
	v_cmp_gt_i32_e64 s[16:17], 64, v27
	s_and_b64 vcc, vcc, s[16:17]
	v_cndmask_b32_e64 v67, 0, 1, vcc
	v_cndmask_b32_e32 v59, 0, v43, vcc
	v_lshl_add_u32 v59, v27, 14, v59
	v_lshlrev_b32_e32 v59, 2, v59
	global_load_dword v51, v59, s[12:13]
	v_lshlrev_b32_e32 v44, 8, v28
	v_sub_u32_e32 v52, v52, v44
	v_add_u32_e32 v44, v44, v6
	v_cmp_lt_i32_e32 vcc, v6, v52
	v_cmp_gt_i32_e64 s[16:17], 64, v29
	s_and_b64 vcc, vcc, s[16:17]
	v_cndmask_b32_e64 v68, 0, 1, vcc
	v_cndmask_b32_e32 v60, 0, v44, vcc
	v_lshl_add_u32 v60, v29, 14, v60
	v_lshlrev_b32_e32 v60, 2, v60
	global_load_dword v52, v60, s[12:13]
	v_lshlrev_b32_e32 v45, 8, v30
	v_sub_u32_e32 v53, v53, v45
	v_add_u32_e32 v45, v45, v6
	v_cmp_lt_i32_e32 vcc, v6, v53
	v_cmp_gt_i32_e64 s[16:17], 64, v31
	s_and_b64 vcc, vcc, s[16:17]
	v_cndmask_b32_e64 v69, 0, 1, vcc
	v_cndmask_b32_e32 v61, 0, v45, vcc
	v_lshl_add_u32 v61, v31, 14, v61
	v_lshlrev_b32_e32 v61, 2, v61
	global_load_dword v53, v61, s[12:13]
	v_lshlrev_b32_e32 v46, 8, v32
	v_sub_u32_e32 v54, v54, v46
	v_add_u32_e32 v46, v46, v6
	v_cmp_lt_i32_e32 vcc, v6, v54
	v_cmp_gt_i32_e64 s[16:17], 64, v33
	s_and_b64 vcc, vcc, s[16:17]
	v_cndmask_b32_e64 v70, 0, 1, vcc
	v_cndmask_b32_e32 v62, 0, v46, vcc
	v_lshl_add_u32 v62, v33, 14, v62
	v_lshlrev_b32_e32 v62, 2, v62
	global_load_dword v54, v62, s[12:13]
	v_lshlrev_b32_e32 v47, 8, v34
	v_sub_u32_e32 v55, v55, v47
	v_add_u32_e32 v47, v47, v6
	v_cmp_lt_i32_e32 vcc, v6, v55
	v_cmp_gt_i32_e64 s[16:17], 64, v35
	s_and_b64 vcc, vcc, s[16:17]
	v_cndmask_b32_e64 v71, 0, 1, vcc
	v_cndmask_b32_e32 v63, 0, v47, vcc
	v_lshl_add_u32 v63, v35, 14, v63
	v_lshlrev_b32_e32 v63, 2, v63
	global_load_dword v55, v63, s[12:13]
	s_waitcnt vmcnt(0)
	v_cmp_ne_u32_e32 vcc, 0, v64
	s_nop 1
	v_cndmask_b32_e32 v48, 0, v48, vcc
	v_cmp_lt_i32_e32 vcc, 63, v21
	s_nop 1
	v_cndmask_b32_e32 v48, v48, v40, vcc
	v_cmp_ne_u32_e32 vcc, 0, v10
	s_and_saveexec_b64 s[16:17], vcc
	ds_write_b32 v9, v48
	s_mov_b64 exec, s[16:17]
	v_cmp_ne_u32_e32 vcc, 0, v65
	s_nop 1
	v_cndmask_b32_e32 v49, 0, v49, vcc
	v_cmp_lt_i32_e32 vcc, 63, v23
	s_nop 1
	v_cndmask_b32_e32 v49, v49, v41, vcc
	v_cmp_ne_u32_e32 vcc, 0, v11
	s_and_saveexec_b64 s[16:17], vcc
	ds_write_b32 v9, v49 offset:2048
	s_mov_b64 exec, s[16:17]
	v_cmp_ne_u32_e32 vcc, 0, v66
	s_nop 1
	v_cndmask_b32_e32 v50, 0, v50, vcc
	v_cmp_lt_i32_e32 vcc, 63, v25
	s_nop 1
	v_cndmask_b32_e32 v50, v50, v42, vcc
	v_cmp_ne_u32_e32 vcc, 0, v12
	s_and_saveexec_b64 s[16:17], vcc
	ds_write_b32 v9, v50 offset:4096
	s_mov_b64 exec, s[16:17]
	v_cmp_ne_u32_e32 vcc, 0, v67
	s_nop 1
	v_cndmask_b32_e32 v51, 0, v51, vcc
	v_cmp_lt_i32_e32 vcc, 63, v27
	s_nop 1
	v_cndmask_b32_e32 v51, v51, v43, vcc
	v_cmp_ne_u32_e32 vcc, 0, v13
	s_and_saveexec_b64 s[16:17], vcc
	ds_write_b32 v9, v51 offset:6144
	s_mov_b64 exec, s[16:17]
	v_cmp_ne_u32_e32 vcc, 0, v68
	s_nop 1
	v_cndmask_b32_e32 v52, 0, v52, vcc
	v_cmp_lt_i32_e32 vcc, 63, v29
	s_nop 1
	v_cndmask_b32_e32 v52, v52, v44, vcc
	v_cmp_ne_u32_e32 vcc, 0, v14
	s_and_saveexec_b64 s[16:17], vcc
	ds_write_b32 v9, v52 offset:8192
	s_mov_b64 exec, s[16:17]
	v_cmp_ne_u32_e32 vcc, 0, v69
	s_nop 1
	v_cndmask_b32_e32 v53, 0, v53, vcc
	v_cmp_lt_i32_e32 vcc, 63, v31
	s_nop 1
	v_cndmask_b32_e32 v53, v53, v45, vcc
	v_cmp_ne_u32_e32 vcc, 0, v15
	s_and_saveexec_b64 s[16:17], vcc
	ds_write_b32 v9, v53 offset:10240
	s_mov_b64 exec, s[16:17]
	v_cmp_ne_u32_e32 vcc, 0, v70
	s_nop 1
	v_cndmask_b32_e32 v54, 0, v54, vcc
	v_cmp_lt_i32_e32 vcc, 63, v33
	s_nop 1
	v_cndmask_b32_e32 v54, v54, v46, vcc
	v_cmp_ne_u32_e32 vcc, 0, v16
	s_and_saveexec_b64 s[16:17], vcc
	ds_write_b32 v9, v54 offset:12288
	s_mov_b64 exec, s[16:17]
	v_cmp_ne_u32_e32 vcc, 0, v71
	s_nop 1
	v_cndmask_b32_e32 v55, 0, v55, vcc
	v_cmp_lt_i32_e32 vcc, 63, v35
	s_nop 1
	v_cndmask_b32_e32 v55, v55, v47, vcc
	v_cmp_ne_u32_e32 vcc, 0, v17
	s_and_saveexec_b64 s[16:17], vcc
	ds_write_b32 v9, v55 offset:14336
	s_mov_b64 exec, s[16:17]
